# attention MFMA sections: one lgkmcnt wait per two MFMAs instead of one per MFMA
# baseline (speedup 1.0000x reference)
; #define ATT_SBAR() __builtin_amdgcn_sched_barrier(0)
; #define ATT_PK4(P, BASE, OUT) do { u32x4 w = {cvtpk(P[BASE + 0], P[BASE + 1]), cvtpk(P[BASE + 2], P[BASE + 3]), cvtpk(P[BASE + 4], P[BASE + 5]), cvtpk(P[BASE + 6], P[BASE + 7])}; \
;     OUT = *reinterpret_cast<bf16x8*>(&w); } while (0)
; #define ATT_WRITE_K(so) do { *(bf16x8*)(K_lds + (so) + kswz<DQK>(kr, kc * 2)) = sk0; if constexpr (DQK == 128) *(bf16x8*)(K_lds + (so) + kswz<DQK>(32 + kr, kc * 2)) = sk1; } while (0)
; #define ATT_WRITE_V(so) do { *(bf16x8*)(V_lds + (so) + vst0) = sv0; *(bf16x8*)(V_lds + (so) + vst1) = sv1; } while (0)
; #define ATT_BAR() do { ATT_SBAR(); asm volatile("s_barrier" ::: "memory"); ATT_SBAR(); } while (0)
; #define ATT_VPAIR(buf, so, blk, ks) do { if constexpr (!(ABL & 8) && !(ABL & 32)) { buf[2 * (ks)] = vtr(vq0 + (so) + v_rd_off(blk, ks, 0)); buf[2 * (ks) + 1] = vtr(vq0 + (so) + v_rd_off(blk, ks, 1)); } } while (0)
; __device__ __forceinline__ void softmax_exp_pack(f32x16& p0, f32x16& p1, bf16x8& pa0, bf16x8& pa1, bf16x8& pa2, bf16x8& pa3) {
; #pragma unroll
;   for (int r = 0; r < 16; ++r) { p0[r] = __builtin_amdgcn_exp2f(p0[r]); p1[r] = __builtin_amdgcn_exp2f(p1[r]); }
;     ...
;   ATT_PK4(p0, 0, pa0); ATT_PK4(p0, 8, pa1); ATT_PK4(p1, 0, pa2); ATT_PK4(p1, 8, pa3);
;     ...
; }
;     ...
;     if constexpr (!(ABL & 4)) { ATT_WRITE_K(k2); ATT_WRITE_V(v1); }
;     ATT_SBAR();
; #pragma unroll
;     for (int ks = 0; ks < 4; ++ks) ATT_VPAIR(va, v0, 0, ks);
;     asm volatile("s_waitcnt lgkmcnt(8)" ::: "memory"); ATT_BAR();
.LBB0_266:
	v_exp_f32_e32 v98, v98
	v_exp_f32_e32 v114, v114
	v_exp_f32_e32 v99, v99
	v_exp_f32_e32 v115, v115
	v_exp_f32_e32 v100, v100
	v_exp_f32_e32 v101, v101
	v_exp_f32_e32 v102, v102
	v_exp_f32_e32 v103, v103
	v_exp_f32_e32 v106, v106
	v_exp_f32_e32 v107, v107
	v_exp_f32_e32 v116, v116
	v_exp_f32_e32 v117, v117
	v_exp_f32_e32 v118, v118
	v_exp_f32_e32 v119, v119
	v_exp_f32_e32 v104, v104
	v_exp_f32_e32 v120, v120
	v_exp_f32_e32 v105, v105
	v_exp_f32_e32 v121, v121
	v_exp_f32_e32 v122, v122
	v_exp_f32_e32 v123, v123
	v_exp_f32_e32 v108, v108
	v_exp_f32_e32 v124, v124
	v_exp_f32_e32 v109, v109
	v_exp_f32_e32 v125, v125
	v_exp_f32_e32 v110, v110
	v_exp_f32_e32 v126, v126
	v_exp_f32_e32 v111, v111
	v_exp_f32_e32 v127, v127
	v_exp_f32_e32 v112, v112
	v_exp_f32_e32 v128, v128
	v_exp_f32_e32 v113, v113
	v_exp_f32_e32 v129, v129
	s_add_i32 s14, s92, 0
	v_cvt_pk_bf16_f32 v98, v98, v99
	v_cvt_pk_bf16_f32 v99, v100, v101
	v_cvt_pk_bf16_f32 v100, v102, v103
	v_cvt_pk_bf16_f32 v102, v106, v107
	v_cvt_pk_bf16_f32 v106, v114, v115
	v_add_u32_e32 v114, s14, v186
	s_add_i32 s14, s93, 0
	s_waitcnt vmcnt(3)
	ds_write_b128 v114, v[224:227] offset:49152
	s_waitcnt vmcnt(2)
	ds_write_b128 v114, v[228:231] offset:57856
	v_add_u32_e32 v114, s14, v189
	v_cvt_pk_bf16_f32 v101, v104, v105
	v_cvt_pk_bf16_f32 v103, v108, v109
	v_cvt_pk_bf16_f32 v104, v110, v111
	v_cvt_pk_bf16_f32 v105, v112, v113
	v_cvt_pk_bf16_f32 v107, v116, v117
	v_cvt_pk_bf16_f32 v108, v118, v119
	v_cvt_pk_bf16_f32 v109, v120, v121
	v_cvt_pk_bf16_f32 v110, v122, v123
	v_cvt_pk_bf16_f32 v111, v124, v125
	v_cvt_pk_bf16_f32 v112, v126, v127
	v_cvt_pk_bf16_f32 v113, v128, v129
	s_waitcnt vmcnt(1)
	ds_write_b128 v114, v[232:235]
	v_add_u32_e32 v114, s14, v190
	s_waitcnt vmcnt(0)
	ds_write_b128 v114, v[236:239]
	v_add_u32_e32 v172, s97, v131
	ds_read_b64_tr_b16 v[114:115], v172
	ds_read_b64_tr_b16 v[116:117], v172 offset:2048
	ds_read_b64_tr_b16 v[118:119], v172 offset:4096
	ds_read_b64_tr_b16 v[120:121], v172 offset:6144
	ds_read_b64_tr_b16 v[122:123], v172 offset:8192
	ds_read_b64_tr_b16 v[124:125], v172 offset:10240
	ds_read_b64_tr_b16 v[126:127], v172 offset:12288
	ds_read_b64_tr_b16 v[128:129], v172 offset:14336
	s_waitcnt lgkmcnt(8)
	s_barrier
; #define ATT_SBAR() __builtin_amdgcn_sched_barrier(0)
; __device__ __forceinline__ unsigned cvtpk(float lo, float hi) { f32x2_t v = {lo, hi}; bf16x2_t b = __builtin_convertvector(v, bf16x2_t); return __builtin_bit_cast(unsigned, b); }
; #define ATT_LOAD_K(t) do { const unsigned so_ = (unsigned)(t) * (unsigned)(KVBLK * LDK * 2); sk0 = __builtin_bit_cast(bf16x8, __builtin_amdgcn_raw_buffer_load_b128(krs, koff, so_, 0)); \
;     if constexpr (DQK == 128) sk1 = __builtin_bit_cast(bf16x8, __builtin_amdgcn_raw_buffer_load_b128(krs, koff, so_ + (unsigned)(32 * LDK * 2), 0)); } while (0)
; #define ATT_LOAD_V(t) do { const unsigned so_ = (unsigned)(t) * (unsigned)(KVBLK * LDV * 2); sv0 = __builtin_bit_cast(bf16x8, __builtin_amdgcn_raw_buffer_load_b128(vrs, voff, so_, 0)); \
;     sv1 = __builtin_bit_cast(bf16x8, __builtin_amdgcn_raw_buffer_load_b128(vrs, voff, so_ + (unsigned)(32 * LDV * 2), 0)); } while (0)
; #define ATT_WRITE_K(so) do { *(bf16x8*)(K_lds + (so) + kswz<DQK>(kr, kc * 2)) = sk0; if constexpr (DQK == 128) *(bf16x8*)(K_lds + (so) + kswz<DQK>(32 + kr, kc * 2)) = sk1; } while (0)
;     ...
;   for (int t = 0; t + 1 < NT; ++t) {
;     if constexpr (ABL & 1) { u32x4 w0 = {cvtpk(p0[0], p0[1]), cvtpk(p0[2], p0[3]), cvtpk(p0[4], p0[5]), cvtpk(p0[6], p0[7])}, w1 = {cvtpk(p0[8], p0[9]), cvtpk(p0[10], p0[11]), cvtpk(p0[12], p0[13]), cvtpk(p0[14], p0[15])};
;         u32x4 w2 = {cvtpk(p1[0], p1[1]), cvtpk(p1[2], p1[3]), cvtpk(p1[4], p1[5]), cvtpk(p1[6], p1[7])}, w3 = {cvtpk(p1[8], p1[9]), cvtpk(p1[10], p1[11]), cvtpk(p1[12], p1[13]), cvtpk(p1[14], p1[15])};
;         pa0 = *reinterpret_cast<bf16x8*>(&w0); pa1 = *reinterpret_cast<bf16x8*>(&w1); pa2 = *reinterpret_cast<bf16x8*>(&w2); pa3 = *reinterpret_cast<bf16x8*>(&w3); }
;     else { ATT_SOFTMAX(t == 0); }
;     if constexpr (!(ABL & 4)) { ATT_WRITE_K(k2); ATT_WRITE_V(v1); }
;     ATT_SBAR();
; #pragma unroll
;     for (int ks = 0; ks < 4; ++ks) ATT_VPAIR(va, v0, 0, ks);
;     asm volatile("s_waitcnt lgkmcnt(8)" ::: "memory"); ATT_BAR();
;     ATT_XSECTION(true);
;     if constexpr (!(ABL & 4)) { const int tk = (t + 3 < NT) ? t + 3 : NT - 1, tv = (t + 2 < NT) ? t + 2 : NT - 1; ATT_LOAD_K(tk); ATT_LOAD_V(tv); }
;     ATT_BAR();
;     { const int tk_ = k0; k0 = k1; k1 = k2; k2 = tk_; const int tv_ = v0; v0 = v1; v1 = v2; v2 = tv_; }
	s_setprio 2
	s_waitcnt lgkmcnt(4)
	v_mfma_f32_32x32x16_bf16 v[18:33], v[98:101], v[114:117], v[18:33]
	ds_read_b64_tr_b16 v[168:169], v172 offset:512
	ds_read_b64_tr_b16 v[170:171], v172 offset:2560
	v_mfma_f32_32x32x16_bf16 v[18:33], v[102:105], v[118:121], v[18:33]
	ds_read_b64_tr_b16 v[114:115], v172 offset:4608
	ds_read_b64_tr_b16 v[116:117], v172 offset:6656
	s_waitcnt lgkmcnt(4)
	v_mfma_f32_32x32x16_bf16 v[18:33], v[106:109], v[122:125], v[18:33]
	ds_read_b64_tr_b16 v[118:119], v172 offset:8704
	ds_read_b64_tr_b16 v[120:121], v172 offset:10752
	v_mfma_f32_32x32x16_bf16 v[18:33], v[110:113], v[126:129], v[18:33]
	ds_read_b64_tr_b16 v[122:123], v172 offset:12800
	ds_read_b64_tr_b16 v[124:125], v172 offset:14848
	s_waitcnt lgkmcnt(4)
	v_mfma_f32_32x32x16_bf16 v[34:49], v[98:101], v[168:171], v[34:49]
	ds_read_b64_tr_b16 v[126:127], v172 offset:1024
	ds_read_b64_tr_b16 v[128:129], v172 offset:3072
	v_mfma_f32_32x32x16_bf16 v[34:49], v[102:105], v[114:117], v[34:49]
	ds_read_b64_tr_b16 v[168:169], v172 offset:5120
	ds_read_b64_tr_b16 v[170:171], v172 offset:7168
	s_waitcnt lgkmcnt(4)
	v_mfma_f32_32x32x16_bf16 v[34:49], v[106:109], v[118:121], v[34:49]
	ds_read_b64_tr_b16 v[114:115], v172 offset:9216
	ds_read_b64_tr_b16 v[116:117], v172 offset:11264
	v_mfma_f32_32x32x16_bf16 v[34:49], v[110:113], v[122:125], v[34:49]
	ds_read_b64_tr_b16 v[118:119], v172 offset:13312
	ds_read_b64_tr_b16 v[120:121], v172 offset:15360
	s_waitcnt lgkmcnt(4)
	v_mfma_f32_32x32x16_bf16 v[50:65], v[98:101], v[126:129], v[50:65]
	ds_read_b64_tr_b16 v[122:123], v172 offset:1536
	ds_read_b64_tr_b16 v[124:125], v172 offset:3584
	v_mfma_f32_32x32x16_bf16 v[50:65], v[102:105], v[168:171], v[50:65]
	ds_read_b64_tr_b16 v[126:127], v172 offset:5632
	ds_read_b64_tr_b16 v[128:129], v172 offset:7680
	s_waitcnt lgkmcnt(4)
	v_mfma_f32_32x32x16_bf16 v[50:65], v[106:109], v[114:117], v[50:65]
	ds_read_b64_tr_b16 v[168:169], v172 offset:9728
	ds_read_b64_tr_b16 v[170:171], v172 offset:11776
	v_mfma_f32_32x32x16_bf16 v[50:65], v[110:113], v[118:121], v[50:65]
	ds_read_b64_tr_b16 v[114:115], v172 offset:13824
	ds_read_b64_tr_b16 v[116:117], v172 offset:15872
	s_waitcnt lgkmcnt(4)
	v_mfma_f32_32x32x16_bf16 v[66:81], v[98:101], v[122:125], v[66:81]
	v_add_u32_e32 v193, s36, v192
	ds_read_b128 v[118:121], v193 offset:49152
	v_mfma_f32_32x32x16_bf16 v[66:81], v[102:105], v[126:129], v[66:81]
	ds_read_b128 v[172:175], v193 offset:57856
	s_waitcnt lgkmcnt(2)
	v_mfma_f32_32x32x16_bf16 v[66:81], v[106:109], v[168:171], v[66:81]
	ds_read_b128 v[176:179], v193 offset:49184
	v_mfma_f32_32x32x16_bf16 v[66:81], v[110:113], v[114:117], v[66:81]
	ds_read_b128 v[168:171], v193 offset:57888
	v_mfma_f32_4x4x4_16b_bf16 v[240:243], v[98:99], v[132:133], v[240:243]
	ds_read_b128 v[180:183], v193 offset:49216
	v_mfma_f32_4x4x4_16b_bf16 v[244:247], v[100:101], v[132:133], v[244:247]
	v_mfma_f32_4x4x4_16b_bf16 v[240:243], v[102:103], v[132:133], v[240:243]
	ds_read_b128 v[194:197], v193 offset:57920
	v_mfma_f32_4x4x4_16b_bf16 v[244:247], v[104:105], v[132:133], v[244:247]
	v_mfma_f32_4x4x4_16b_bf16 v[240:243], v[106:107], v[132:133], v[240:243]
	ds_read_b128 v[198:201], v193 offset:49248
	v_mfma_f32_4x4x4_16b_bf16 v[244:247], v[108:109], v[132:133], v[244:247]
	v_mfma_f32_4x4x4_16b_bf16 v[240:243], v[110:111], v[132:133], v[240:243]
	ds_read_b128 v[212:215], v193 offset:57952
	v_mfma_f32_4x4x4_16b_bf16 v[244:247], v[112:113], v[132:133], v[244:247]
	s_waitcnt lgkmcnt(6)
	v_mfma_f32_32x32x16_bf16 v[98:113], v[118:121], v[136:139], v[82:97]
	ds_read_b128 v[216:219], v193 offset:49280
	v_mfma_f32_32x32x16_bf16 v[114:129], v[172:175], v[136:139], v[82:97]
	ds_read_b128 v[220:223], v193 offset:57984
	s_waitcnt lgkmcnt(6)
	v_mfma_f32_32x32x16_bf16 v[98:113], v[176:179], v[140:143], v[98:113]
	ds_read_b128 v[172:175], v193 offset:49312
	v_mfma_f32_32x32x16_bf16 v[114:129], v[168:171], v[140:143], v[114:129]
	ds_read_b128 v[176:179], v193 offset:58016
	s_waitcnt lgkmcnt(6)
	v_mfma_f32_32x32x16_bf16 v[98:113], v[180:183], v[144:147], v[98:113]
	ds_read_b128 v[168:171], v193 offset:49344
	v_mfma_f32_32x32x16_bf16 v[114:129], v[194:197], v[144:147], v[114:129]
	ds_read_b128 v[180:183], v193 offset:58048
	s_waitcnt lgkmcnt(6)
	v_mfma_f32_32x32x16_bf16 v[98:113], v[198:201], v[148:151], v[98:113]
	ds_read_b128 v[194:197], v193 offset:49376
	v_mfma_f32_32x32x16_bf16 v[114:129], v[212:215], v[148:151], v[114:129]
	ds_read_b128 v[198:201], v193 offset:58080
	s_waitcnt lgkmcnt(6)
	v_mfma_f32_32x32x16_bf16 v[98:113], v[216:219], v[152:155], v[98:113]
	s_min_u32 s14, s95, 0x7c
	s_lshl_b32 s14, s14, 15
	s_add_i32 s15, s14, 0x18000
	s_add_i32 s14, s14, 0x1c000
	buffer_load_dwordx4 v[224:227], v191, s[8:11], s15 offen
	v_mfma_f32_32x32x16_bf16 v[114:129], v[220:223], v[152:155], v[114:129]
	buffer_load_dwordx4 v[228:231], v191, s[8:11], s14 offen
	s_waitcnt lgkmcnt(4)
	v_mfma_f32_32x32x16_bf16 v[98:113], v[172:175], v[156:159], v[98:113]
	s_add_i32 s18, s96, 0xffffc000
	s_mov_b32 s14, s10
	s_mov_b32 s15, s11
	buffer_load_dwordx4 v[232:235], v191, s[12:15], s18 offen
	v_mfma_f32_32x32x16_bf16 v[114:129], v[176:179], v[156:159], v[114:129]
	buffer_load_dwordx4 v[236:239], v191, s[12:15], s96 offen
	s_waitcnt lgkmcnt(2)
	v_mfma_f32_32x32x16_bf16 v[98:113], v[168:171], v[160:163], v[98:113]
	v_mfma_f32_32x32x16_bf16 v[114:129], v[180:183], v[160:163], v[114:129]
	s_waitcnt lgkmcnt(0)
	v_mfma_f32_32x32x16_bf16 v[98:113], v[194:197], v[164:167], v[98:113]
	v_mfma_f32_32x32x16_bf16 v[114:129], v[198:201], v[164:167], v[114:129]
	s_setprio 0
	s_barrier
	s_add_i32 s96, s96, 0x8000
	s_add_i32 s95, s95, 1
	s_cmpk_eq_i32 s95, 0x7e
	s_cbranch_scc1 .LBB0_274
	s_mov_b32 s14, s92
	s_mov_b32 s92, s94
	s_mov_b32 s94, s36
	s_mov_b32 s15, s93
	s_mov_b32 s93, s91
	s_mov_b32 s91, s97
	s_branch .LBB0_265

; #define ATT_SBAR() __builtin_amdgcn_sched_barrier(0)
; #define ATT_PK4(P, BASE, OUT) do { u32x4 w = {cvtpk(P[BASE + 0], P[BASE + 1]), cvtpk(P[BASE + 2], P[BASE + 3]), cvtpk(P[BASE + 4], P[BASE + 5]), cvtpk(P[BASE + 6], P[BASE + 7])}; \
;     OUT = *reinterpret_cast<bf16x8*>(&w); } while (0)
; #define ATT_WRITE_K(so) do { *(bf16x8*)(K_lds + (so) + kswz<DQK>(kr, kc * 2)) = sk0; if constexpr (DQK == 128) *(bf16x8*)(K_lds + (so) + kswz<DQK>(32 + kr, kc * 2)) = sk1; } while (0)
; #define ATT_WRITE_V(so) do { *(bf16x8*)(V_lds + (so) + vst0) = sv0; *(bf16x8*)(V_lds + (so) + vst1) = sv1; } while (0)
; #define ATT_BAR() do { ATT_SBAR(); asm volatile("s_barrier" ::: "memory"); ATT_SBAR(); } while (0)
; #define ATT_VPAIR(buf, so, blk, ks) do { if constexpr (!(ABL & 8) && !(ABL & 32)) { buf[2 * (ks)] = vtr(vq0 + (so) + v_rd_off(blk, ks, 0)); buf[2 * (ks) + 1] = vtr(vq0 + (so) + v_rd_off(blk, ks, 1)); } } while (0)
; __device__ __forceinline__ void softmax_exp_pack(f32x16& p0, f32x16& p1, bf16x8& pa0, bf16x8& pa1, bf16x8& pa2, bf16x8& pa3) {
; #pragma unroll
;   for (int r = 0; r < 16; ++r) { p0[r] = __builtin_amdgcn_exp2f(p0[r]); p1[r] = __builtin_amdgcn_exp2f(p1[r]); }
;     ...
;   ATT_PK4(p0, 0, pa0); ATT_PK4(p0, 8, pa1); ATT_PK4(p1, 0, pa2); ATT_PK4(p1, 8, pa3);
;     ...
; }
;     ...
;     if constexpr (!(ABL & 4)) { ATT_WRITE_K(k2); ATT_WRITE_V(v1); }
;     ATT_SBAR();
; #pragma unroll
;     for (int ks = 0; ks < 4; ++ks) ATT_VPAIR(va, v0, 0, ks);
;     asm volatile("s_waitcnt lgkmcnt(8)" ::: "memory"); ATT_BAR();
.LBB0_283:
	v_exp_f32_e32 v98, v98
	v_exp_f32_e32 v114, v114
	v_exp_f32_e32 v99, v99
	v_exp_f32_e32 v115, v115
	v_exp_f32_e32 v100, v100
	v_exp_f32_e32 v101, v101
	v_exp_f32_e32 v102, v102
	v_exp_f32_e32 v103, v103
	v_exp_f32_e32 v106, v106
	v_exp_f32_e32 v107, v107
	v_exp_f32_e32 v116, v116
	v_exp_f32_e32 v117, v117
	v_exp_f32_e32 v118, v118
	v_exp_f32_e32 v119, v119
	v_exp_f32_e32 v104, v104
	v_exp_f32_e32 v120, v120
	v_exp_f32_e32 v105, v105
	v_exp_f32_e32 v121, v121
	v_exp_f32_e32 v122, v122
	v_exp_f32_e32 v123, v123
	v_exp_f32_e32 v108, v108
	v_exp_f32_e32 v124, v124
	v_exp_f32_e32 v109, v109
	v_exp_f32_e32 v125, v125
	v_exp_f32_e32 v110, v110
	v_exp_f32_e32 v126, v126
	v_exp_f32_e32 v111, v111
	v_exp_f32_e32 v127, v127
	v_exp_f32_e32 v112, v112
	v_exp_f32_e32 v128, v128
	v_exp_f32_e32 v113, v113
	v_exp_f32_e32 v129, v129
	v_cvt_pk_bf16_f32 v2, v98, v99
	v_cvt_pk_bf16_f32 v3, v100, v101
	v_cvt_pk_bf16_f32 v4, v102, v103
	v_cvt_pk_bf16_f32 v6, v106, v107
	v_cvt_pk_bf16_f32 v10, v114, v115
	v_add_u32_e32 v114, s94, v169
	s_add_i32 s14, s95, 0
	s_waitcnt vmcnt(2)
	ds_write_b128 v114, v[224:227] offset:49152
	v_add_u32_e32 v114, s14, v167
	v_cvt_pk_bf16_f32 v5, v104, v105
	v_cvt_pk_bf16_f32 v7, v108, v109
	v_cvt_pk_bf16_f32 v8, v110, v111
	v_cvt_pk_bf16_f32 v9, v112, v113
	v_cvt_pk_bf16_f32 v11, v116, v117
	v_cvt_pk_bf16_f32 v12, v118, v119
	v_cvt_pk_bf16_f32 v13, v120, v121
	v_cvt_pk_bf16_f32 v14, v122, v123
	v_cvt_pk_bf16_f32 v15, v124, v125
	v_cvt_pk_bf16_f32 v16, v126, v127
	v_cvt_pk_bf16_f32 v17, v128, v129
	s_waitcnt vmcnt(1)
	ds_write_b128 v114, v[228:231]
	v_add_u32_e32 v114, s14, v168
	s_waitcnt vmcnt(0)
	ds_write_b128 v114, v[232:235]
	v_add_u32_e32 v249, s96, v172
	ds_read_b128 v[152:155], v249 offset:49152
	ds_read_b128 v[156:159], v249 offset:53760
	ds_read_b128 v[160:163], v249 offset:49184
	ds_read_b128 v[176:179], v249 offset:53792
	s_waitcnt lgkmcnt(4)
	s_barrier
; #define ATT_SBAR() __builtin_amdgcn_sched_barrier(0)
; __device__ __forceinline__ float softmax_rowmax(const f32x16& p0, const f32x16& p1) {
;   const float m0 = p1[0] + 0.0f; float a, b;
;   asm("v_max3_f32 %0, %1, %2, %3\n\tv_max3_f32 %0, %0, %4, %5\n\tv_max3_f32 %0, %0, %6, %7\n\tv_max3_f32 %0, %0, %8, %9\n\t"
;       "v_max3_f32 %0, %0, %10, %11\n\tv_max3_f32 %0, %0, %12, %13\n\tv_max3_f32 %0, %0, %14, %15\n\tv_max3_f32 %0, %0, %16, %17"
;       : "=&v"(a) : "v"(m0), "v"(p0[0]), "v"(p0[1]), "v"(p0[2]), "v"(p0[3]), "v"(p0[4]), "v"(p0[5]), "v"(p0[6]), "v"(p0[7]), "v"(p0[8]), "v"(p0[9]), "v"(p0[10]), "v"(p0[11]), "v"(p0[12]), "v"(p0[13]), "v"(p0[14]), "v"(p0[15]));
;   asm("v_max3_f32 %0, %1, %2, %3\n\tv_max3_f32 %0, %0, %4, %5\n\tv_max3_f32 %0, %0, %6, %7\n\tv_max3_f32 %0, %0, %8, %9\n\t"
;       "v_max3_f32 %0, %0, %10, %11\n\tv_max3_f32 %0, %0, %12, %13\n\tv_max3_f32 %0, %0, %14, %15\n\tv_max_f32 %0, %0, %16"
;       : "=&v"(b) : "v"(a), "v"(p1[1]), "v"(p1[2]), "v"(p1[3]), "v"(p1[4]), "v"(p1[5]), "v"(p1[6]), "v"(p1[7]), "v"(p1[8]), "v"(p1[9]), "v"(p1[10]), "v"(p1[11]), "v"(p1[12]), "v"(p1[13]), "v"(p1[14]), "v"(p1[15]));
;   return b;
;     ...
;   for (int t = 0; t + 1 < NT; ++t) {
;     if constexpr (ABL & 1) { u32x4 w0 = {cvtpk(p0[0], p0[1]), cvtpk(p0[2], p0[3]), cvtpk(p0[4], p0[5]), cvtpk(p0[6], p0[7])}, w1 = {cvtpk(p0[8], p0[9]), cvtpk(p0[10], p0[11]), cvtpk(p0[12], p0[13]), cvtpk(p0[14], p0[15])};
;         u32x4 w2 = {cvtpk(p1[0], p1[1]), cvtpk(p1[2], p1[3]), cvtpk(p1[4], p1[5]), cvtpk(p1[6], p1[7])}, w3 = {cvtpk(p1[8], p1[9]), cvtpk(p1[10], p1[11]), cvtpk(p1[12], p1[13]), cvtpk(p1[14], p1[15])};
;         pa0 = *reinterpret_cast<bf16x8*>(&w0); pa1 = *reinterpret_cast<bf16x8*>(&w1); pa2 = *reinterpret_cast<bf16x8*>(&w2); pa3 = *reinterpret_cast<bf16x8*>(&w3); }
;     else { ATT_SOFTMAX(t == 0); }
;     if constexpr (!(ABL & 4)) { ATT_WRITE_K(k2); ATT_WRITE_V(v1); }
;     ATT_SBAR();
; #pragma unroll
;     for (int ks = 0; ks < 4; ++ks) ATT_VPAIR(va, v0, 0, ks);
;     asm volatile("s_waitcnt lgkmcnt(8)" ::: "memory"); ATT_BAR();
;     ATT_XSECTION(true);
;     if constexpr (!(ABL & 4)) { const int tk = (t + 3 < NT) ? t + 3 : NT - 1, tv = (t + 2 < NT) ? t + 2 : NT - 1; ATT_LOAD_K(tk); ATT_LOAD_V(tv); }
;     ATT_BAR();
;     { const int tk_ = k0; k0 = k1; k1 = k2; k2 = tk_; const int tv_ = v0; v0 = v1; v1 = v2; v2 = tv_; }
	s_setprio 2
	s_waitcnt lgkmcnt(2)
	v_mfma_f32_32x32x16_bf16 v[98:113], v[152:155], v[136:139], v[82:97]
	ds_read_b128 v[180:183], v249 offset:49216
	v_mfma_f32_32x32x16_bf16 v[114:129], v[156:159], v[136:139], v[82:97]
	ds_read_b128 v[186:189], v249 offset:53824
	v_add_u32_e32 v248, s37, v131
	s_waitcnt lgkmcnt(2)
	v_mfma_f32_32x32x16_bf16 v[98:113], v[160:163], v[140:143], v[98:113]
	ds_read_b128 v[190:193], v249 offset:49248
	ds_read_b64_tr_b16 v[198:199], v248
	ds_read_b64_tr_b16 v[200:201], v248 offset:2048
	v_mfma_f32_32x32x16_bf16 v[114:129], v[176:179], v[140:143], v[114:129]
	ds_read_b128 v[194:197], v249 offset:53856
	ds_read_b64_tr_b16 v[212:213], v248 offset:4096
	ds_read_b64_tr_b16 v[214:215], v248 offset:6144
	s_waitcnt lgkmcnt(6)
	v_mfma_f32_32x32x16_bf16 v[98:113], v[180:183], v[144:147], v[98:113]
	ds_read_b64_tr_b16 v[216:217], v248 offset:8192
	ds_read_b64_tr_b16 v[218:219], v248 offset:10240
	v_mfma_f32_32x32x16_bf16 v[114:129], v[186:189], v[144:147], v[114:129]
	ds_read_b64_tr_b16 v[220:221], v248 offset:12288
	ds_read_b64_tr_b16 v[222:223], v248 offset:14336
	s_waitcnt lgkmcnt(6)
	v_mfma_f32_32x32x16_bf16 v[98:113], v[190:193], v[148:151], v[98:113]
	v_mfma_f32_32x32x16_bf16 v[114:129], v[194:197], v[148:151], v[114:129]
	v_mfma_f32_32x32x16_bf16 v[18:33], v[2:5], v[198:201], v[18:33]
	ds_read_b64_tr_b16 v[236:237], v248 offset:512
	ds_read_b64_tr_b16 v[238:239], v248 offset:2560
	s_waitcnt lgkmcnt(4)
	v_mfma_f32_32x32x16_bf16 v[18:33], v[6:9], v[212:215], v[18:33]
	ds_read_b64_tr_b16 v[198:199], v248 offset:4608
	ds_read_b64_tr_b16 v[200:201], v248 offset:6656
	v_mfma_f32_32x32x16_bf16 v[18:33], v[10:13], v[216:219], v[18:33]
	ds_read_b64_tr_b16 v[212:213], v248 offset:8704
	ds_read_b64_tr_b16 v[214:215], v248 offset:10752
	s_waitcnt lgkmcnt(4)
	v_mfma_f32_32x32x16_bf16 v[18:33], v[14:17], v[220:223], v[18:33]
	ds_read_b64_tr_b16 v[216:217], v248 offset:12800
	ds_read_b64_tr_b16 v[218:219], v248 offset:14848
	v_max3_f32 v249, v98, v99, v100
	v_mfma_f32_32x32x16_bf16 v[34:49], v[2:5], v[236:239], v[34:49]
	ds_read_b64_tr_b16 v[220:221], v248 offset:1024
	ds_read_b64_tr_b16 v[222:223], v248 offset:3072
	v_max3_f32 v173, v114, v115, v116
	s_waitcnt lgkmcnt(4)
	v_mfma_f32_32x32x16_bf16 v[34:49], v[6:9], v[198:201], v[34:49]
	ds_read_b64_tr_b16 v[236:237], v248 offset:5120
	ds_read_b64_tr_b16 v[238:239], v248 offset:7168
	v_max3_f32 v249, v249, v101, v102
	v_mfma_f32_32x32x16_bf16 v[34:49], v[10:13], v[212:215], v[34:49]
	ds_read_b64_tr_b16 v[198:199], v248 offset:9216
	ds_read_b64_tr_b16 v[200:201], v248 offset:11264
	v_max3_f32 v173, v173, v117, v118
	s_waitcnt lgkmcnt(4)
	v_mfma_f32_32x32x16_bf16 v[34:49], v[14:17], v[216:219], v[34:49]
	ds_read_b64_tr_b16 v[212:213], v248 offset:13312
	ds_read_b64_tr_b16 v[214:215], v248 offset:15360
	v_max3_f32 v249, v249, v103, v104
	v_mfma_f32_32x32x16_bf16 v[50:65], v[2:5], v[220:223], v[50:65]
	ds_read_b64_tr_b16 v[216:217], v248 offset:1536
	ds_read_b64_tr_b16 v[218:219], v248 offset:3584
	v_max3_f32 v173, v173, v119, v120
	s_waitcnt lgkmcnt(4)
	v_mfma_f32_32x32x16_bf16 v[50:65], v[6:9], v[236:239], v[50:65]
	ds_read_b64_tr_b16 v[220:221], v248 offset:5632
	ds_read_b64_tr_b16 v[222:223], v248 offset:7680
	v_max3_f32 v249, v249, v105, v106
	v_mfma_f32_32x32x16_bf16 v[50:65], v[10:13], v[198:201], v[50:65]
	ds_read_b64_tr_b16 v[236:237], v248 offset:9728
	ds_read_b64_tr_b16 v[238:239], v248 offset:11776
	v_max3_f32 v173, v173, v121, v122
	s_waitcnt lgkmcnt(4)
	v_mfma_f32_32x32x16_bf16 v[50:65], v[14:17], v[212:215], v[50:65]
	ds_read_b64_tr_b16 v[198:199], v248 offset:13824
	ds_read_b64_tr_b16 v[200:201], v248 offset:15872
	v_max3_f32 v249, v249, v107, v108
	v_mfma_f32_32x32x16_bf16 v[66:81], v[2:5], v[216:219], v[66:81]
	v_max3_f32 v173, v173, v123, v124
	s_min_u32 s14, s97, 0x7c
	s_lshl_b32 s14, s14, 17
	s_add_i32 s14, s14, 0x60000
	buffer_load_dwordx4 v[224:227], v170, s[8:11], s14 offen
	s_waitcnt lgkmcnt(2)
	v_mfma_f32_32x32x16_bf16 v[66:81], v[6:9], v[220:223], v[66:81]
	v_max3_f32 v249, v249, v109, v110
	s_add_i32 s19, s36, 0xffff0000
	s_mov_b32 s14, s10
	s_mov_b32 s15, s11
	buffer_load_dwordx4 v[228:231], v171, s[12:15], s19 offen
	v_mfma_f32_32x32x16_bf16 v[66:81], v[10:13], v[236:239], v[66:81]
	v_max3_f32 v173, v173, v125, v126
	buffer_load_dwordx4 v[232:235], v171, s[12:15], s36 offen
	s_waitcnt lgkmcnt(0)
	v_mfma_f32_32x32x16_bf16 v[66:81], v[14:17], v[198:201], v[66:81]
	v_max3_f32 v249, v249, v111, v112
	v_mfma_f32_4x4x4_16b_bf16 v[240:243], v[2:3], v[132:133], v[240:243]
	v_max3_f32 v173, v173, v127, v128
	v_mfma_f32_4x4x4_16b_bf16 v[244:247], v[4:5], v[132:133], v[244:247]
	v_mfma_f32_4x4x4_16b_bf16 v[240:243], v[6:7], v[132:133], v[240:243]
	v_max_f32 v249, v249, v113
	v_mfma_f32_4x4x4_16b_bf16 v[244:247], v[8:9], v[132:133], v[244:247]
	v_mfma_f32_4x4x4_16b_bf16 v[240:243], v[10:11], v[132:133], v[240:243]
	v_max_f32 v173, v173, v129
	v_mfma_f32_4x4x4_16b_bf16 v[244:247], v[12:13], v[132:133], v[244:247]
	v_mfma_f32_4x4x4_16b_bf16 v[240:243], v[14:15], v[132:133], v[240:243]
	v_max_f32 v173, v173, v249
	v_mfma_f32_4x4x4_16b_bf16 v[244:247], v[16:17], v[132:133], v[244:247]
	s_setprio 0
	s_barrier
	s_add_i32 s36, s36, 0x20000
	s_add_i32 s97, s97, 1
	s_cmpk_eq_i32 s97, 0x7e
	s_cbranch_scc1 .LBB0_290
	s_mov_b32 s14, s94
	s_mov_b32 s94, s18
	s_mov_b32 s18, s96
	s_mov_b32 s15, s95
	s_mov_b32 s95, s93
	s_mov_b32 s93, s37
	s_branch .LBB0_282

; #define ATT_SBAR() __builtin_amdgcn_sched_barrier(0)
; #define ATT_PK4(P, BASE, OUT) do { u32x4 w = {cvtpk(P[BASE + 0], P[BASE + 1]), cvtpk(P[BASE + 2], P[BASE + 3]), cvtpk(P[BASE + 4], P[BASE + 5]), cvtpk(P[BASE + 6], P[BASE + 7])}; \
;     OUT = *reinterpret_cast<bf16x8*>(&w); } while (0)
; #define ATT_WRITE_K(so) do { *(bf16x8*)(K_lds + (so) + kswz<DQK>(kr, kc * 2)) = sk0; if constexpr (DQK == 128) *(bf16x8*)(K_lds + (so) + kswz<DQK>(32 + kr, kc * 2)) = sk1; } while (0)
; #define ATT_WRITE_V(so) do { *(bf16x8*)(V_lds + (so) + vst0) = sv0; *(bf16x8*)(V_lds + (so) + vst1) = sv1; } while (0)
; #define ATT_BAR() do { ATT_SBAR(); asm volatile("s_barrier" ::: "memory"); ATT_SBAR(); } while (0)
; #define ATT_VPAIR(buf, so, blk, ks) do { if constexpr (!(ABL & 8) && !(ABL & 32)) { buf[2 * (ks)] = vtr(vq0 + (so) + v_rd_off(blk, ks, 0)); buf[2 * (ks) + 1] = vtr(vq0 + (so) + v_rd_off(blk, ks, 1)); } } while (0)
; __device__ __forceinline__ void softmax_exp_pack(f32x16& p0, f32x16& p1, bf16x8& pa0, bf16x8& pa1, bf16x8& pa2, bf16x8& pa3) {
; #pragma unroll
;   for (int r = 0; r < 16; ++r) { p0[r] = __builtin_amdgcn_exp2f(p0[r]); p1[r] = __builtin_amdgcn_exp2f(p1[r]); }
;     ...
;   ATT_PK4(p0, 0, pa0); ATT_PK4(p0, 8, pa1); ATT_PK4(p1, 0, pa2); ATT_PK4(p1, 8, pa3);
;     ...
; }
;     ...
;     if constexpr (!(ABL & 4)) { ATT_WRITE_K(k2); ATT_WRITE_V(v1); }
;     ATT_SBAR();
; #pragma unroll
;     for (int ks = 0; ks < 4; ++ks) ATT_VPAIR(va, v0, 0, ks);
;     asm volatile("s_waitcnt lgkmcnt(8)" ::: "memory"); ATT_BAR();
.LBB0_298:
	v_exp_f32_e32 v98, v98
	v_exp_f32_e32 v114, v114
	v_exp_f32_e32 v99, v99
	v_exp_f32_e32 v115, v115
	v_exp_f32_e32 v100, v100
	v_exp_f32_e32 v101, v101
	v_exp_f32_e32 v102, v102
	v_exp_f32_e32 v103, v103
	v_exp_f32_e32 v106, v106
	v_exp_f32_e32 v107, v107
	v_exp_f32_e32 v116, v116
	v_exp_f32_e32 v117, v117
	v_exp_f32_e32 v118, v118
	v_exp_f32_e32 v119, v119
	v_exp_f32_e32 v104, v104
	v_exp_f32_e32 v120, v120
	v_exp_f32_e32 v105, v105
	v_exp_f32_e32 v121, v121
	v_exp_f32_e32 v122, v122
	v_exp_f32_e32 v123, v123
	v_exp_f32_e32 v108, v108
	v_exp_f32_e32 v124, v124
	v_exp_f32_e32 v109, v109
	v_exp_f32_e32 v125, v125
	v_exp_f32_e32 v110, v110
	v_exp_f32_e32 v126, v126
	v_exp_f32_e32 v111, v111
	v_exp_f32_e32 v127, v127
	v_exp_f32_e32 v112, v112
	v_exp_f32_e32 v128, v128
	v_exp_f32_e32 v113, v113
	v_exp_f32_e32 v129, v129
	v_cvt_pk_bf16_f32 v18, v98, v99
	v_cvt_pk_bf16_f32 v19, v100, v101
	v_cvt_pk_bf16_f32 v20, v102, v103
	v_cvt_pk_bf16_f32 v22, v106, v107
	v_cvt_pk_bf16_f32 v26, v114, v115
	v_add_u32_e32 v114, s49, v170
	s_add_i32 s14, s50, 0
	s_waitcnt vmcnt(2)
	ds_write_b128 v114, v[224:227] offset:49152
	v_add_u32_e32 v114, s14, v168
	v_cvt_pk_bf16_f32 v21, v104, v105
	v_cvt_pk_bf16_f32 v23, v108, v109
	v_cvt_pk_bf16_f32 v24, v110, v111
	v_cvt_pk_bf16_f32 v25, v112, v113
	v_cvt_pk_bf16_f32 v27, v116, v117
	v_cvt_pk_bf16_f32 v28, v118, v119
	v_cvt_pk_bf16_f32 v29, v120, v121
	v_cvt_pk_bf16_f32 v30, v122, v123
	v_cvt_pk_bf16_f32 v31, v124, v125
	v_cvt_pk_bf16_f32 v32, v126, v127
	v_cvt_pk_bf16_f32 v33, v128, v129
	s_waitcnt vmcnt(1)
	ds_write_b128 v114, v[228:231]
	v_add_u32_e32 v114, s14, v169
	s_waitcnt vmcnt(0)
	ds_write_b128 v114, v[232:235]
	v_add_u32_e32 v249, s18, v173
	ds_read_b128 v[152:155], v249 offset:49152
	ds_read_b128 v[156:159], v249 offset:53760
	ds_read_b128 v[160:163], v249 offset:49184
	ds_read_b128 v[176:179], v249 offset:53792
	s_waitcnt lgkmcnt(4)
	s_barrier
; #define ATT_SBAR() __builtin_amdgcn_sched_barrier(0)
; __device__ __forceinline__ float softmax_rowmax(const f32x16& p0, const f32x16& p1) {
;   const float m0 = p1[0] + 0.0f; float a, b;
;   asm("v_max3_f32 %0, %1, %2, %3\n\tv_max3_f32 %0, %0, %4, %5\n\tv_max3_f32 %0, %0, %6, %7\n\tv_max3_f32 %0, %0, %8, %9\n\t"
;       "v_max3_f32 %0, %0, %10, %11\n\tv_max3_f32 %0, %0, %12, %13\n\tv_max3_f32 %0, %0, %14, %15\n\tv_max3_f32 %0, %0, %16, %17"
;       : "=&v"(a) : "v"(m0), "v"(p0[0]), "v"(p0[1]), "v"(p0[2]), "v"(p0[3]), "v"(p0[4]), "v"(p0[5]), "v"(p0[6]), "v"(p0[7]), "v"(p0[8]), "v"(p0[9]), "v"(p0[10]), "v"(p0[11]), "v"(p0[12]), "v"(p0[13]), "v"(p0[14]), "v"(p0[15]));
;   asm("v_max3_f32 %0, %1, %2, %3\n\tv_max3_f32 %0, %0, %4, %5\n\tv_max3_f32 %0, %0, %6, %7\n\tv_max3_f32 %0, %0, %8, %9\n\t"
;       "v_max3_f32 %0, %0, %10, %11\n\tv_max3_f32 %0, %0, %12, %13\n\tv_max3_f32 %0, %0, %14, %15\n\tv_max_f32 %0, %0, %16"
;       : "=&v"(b) : "v"(a), "v"(p1[1]), "v"(p1[2]), "v"(p1[3]), "v"(p1[4]), "v"(p1[5]), "v"(p1[6]), "v"(p1[7]), "v"(p1[8]), "v"(p1[9]), "v"(p1[10]), "v"(p1[11]), "v"(p1[12]), "v"(p1[13]), "v"(p1[14]), "v"(p1[15]));
;   return b;
;     ...
;   for (int t = 0; t + 1 < NT; ++t) {
;     if constexpr (ABL & 1) { u32x4 w0 = {cvtpk(p0[0], p0[1]), cvtpk(p0[2], p0[3]), cvtpk(p0[4], p0[5]), cvtpk(p0[6], p0[7])}, w1 = {cvtpk(p0[8], p0[9]), cvtpk(p0[10], p0[11]), cvtpk(p0[12], p0[13]), cvtpk(p0[14], p0[15])};
;         u32x4 w2 = {cvtpk(p1[0], p1[1]), cvtpk(p1[2], p1[3]), cvtpk(p1[4], p1[5]), cvtpk(p1[6], p1[7])}, w3 = {cvtpk(p1[8], p1[9]), cvtpk(p1[10], p1[11]), cvtpk(p1[12], p1[13]), cvtpk(p1[14], p1[15])};
;         pa0 = *reinterpret_cast<bf16x8*>(&w0); pa1 = *reinterpret_cast<bf16x8*>(&w1); pa2 = *reinterpret_cast<bf16x8*>(&w2); pa3 = *reinterpret_cast<bf16x8*>(&w3); }
;     else { ATT_SOFTMAX(t == 0); }
;     if constexpr (!(ABL & 4)) { ATT_WRITE_K(k2); ATT_WRITE_V(v1); }
;     ATT_SBAR();
; #pragma unroll
;     for (int ks = 0; ks < 4; ++ks) ATT_VPAIR(va, v0, 0, ks);
;     asm volatile("s_waitcnt lgkmcnt(8)" ::: "memory"); ATT_BAR();
;     ATT_XSECTION(true);
;     if constexpr (!(ABL & 4)) { const int tk = (t + 3 < NT) ? t + 3 : NT - 1, tv = (t + 2 < NT) ? t + 2 : NT - 1; ATT_LOAD_K(tk); ATT_LOAD_V(tv); }
;     ATT_BAR();
;     { const int tk_ = k0; k0 = k1; k1 = k2; k2 = tk_; const int tv_ = v0; v0 = v1; v1 = v2; v2 = tv_; }
	s_setprio 2
	s_waitcnt lgkmcnt(2)
	v_mfma_f32_32x32x16_bf16 v[98:113], v[152:155], v[136:139], v[82:97]
	ds_read_b128 v[180:183], v249 offset:49216
	v_mfma_f32_32x32x16_bf16 v[114:129], v[156:159], v[136:139], v[82:97]
	ds_read_b128 v[186:189], v249 offset:53824
	v_add_u32_e32 v248, s37, v131
	s_waitcnt lgkmcnt(2)
	v_mfma_f32_32x32x16_bf16 v[98:113], v[160:163], v[140:143], v[98:113]
	ds_read_b128 v[190:193], v249 offset:49248
	ds_read_b64_tr_b16 v[198:199], v248
	ds_read_b64_tr_b16 v[200:201], v248 offset:2048
	v_mfma_f32_32x32x16_bf16 v[114:129], v[176:179], v[140:143], v[114:129]
	ds_read_b128 v[194:197], v249 offset:53856
	ds_read_b64_tr_b16 v[212:213], v248 offset:4096
	ds_read_b64_tr_b16 v[214:215], v248 offset:6144
	s_waitcnt lgkmcnt(6)
	v_mfma_f32_32x32x16_bf16 v[98:113], v[180:183], v[144:147], v[98:113]
	ds_read_b64_tr_b16 v[216:217], v248 offset:8192
	ds_read_b64_tr_b16 v[218:219], v248 offset:10240
	v_mfma_f32_32x32x16_bf16 v[114:129], v[186:189], v[144:147], v[114:129]
	ds_read_b64_tr_b16 v[220:221], v248 offset:12288
	ds_read_b64_tr_b16 v[222:223], v248 offset:14336
	s_waitcnt lgkmcnt(6)
	v_mfma_f32_32x32x16_bf16 v[98:113], v[190:193], v[148:151], v[98:113]
	v_mfma_f32_32x32x16_bf16 v[114:129], v[194:197], v[148:151], v[114:129]
	v_mfma_f32_32x32x16_bf16 v[66:81], v[18:21], v[198:201], v[66:81]
	ds_read_b64_tr_b16 v[236:237], v248 offset:512
	ds_read_b64_tr_b16 v[238:239], v248 offset:2560
	s_waitcnt lgkmcnt(4)
	v_mfma_f32_32x32x16_bf16 v[66:81], v[22:25], v[212:215], v[66:81]
	ds_read_b64_tr_b16 v[198:199], v248 offset:4608
	ds_read_b64_tr_b16 v[200:201], v248 offset:6656
	v_mfma_f32_32x32x16_bf16 v[66:81], v[26:29], v[216:219], v[66:81]
	ds_read_b64_tr_b16 v[212:213], v248 offset:8704
	ds_read_b64_tr_b16 v[214:215], v248 offset:10752
	s_waitcnt lgkmcnt(4)
	v_mfma_f32_32x32x16_bf16 v[66:81], v[30:33], v[220:223], v[66:81]
	ds_read_b64_tr_b16 v[216:217], v248 offset:12800
	ds_read_b64_tr_b16 v[218:219], v248 offset:14848
	v_max3_f32 v249, v98, v99, v100
	v_mfma_f32_32x32x16_bf16 v[50:65], v[18:21], v[236:239], v[50:65]
	ds_read_b64_tr_b16 v[220:221], v248 offset:1024
	ds_read_b64_tr_b16 v[222:223], v248 offset:3072
	v_max3_f32 v174, v114, v115, v116
	s_waitcnt lgkmcnt(4)
	v_mfma_f32_32x32x16_bf16 v[50:65], v[22:25], v[198:201], v[50:65]
	ds_read_b64_tr_b16 v[236:237], v248 offset:5120
	ds_read_b64_tr_b16 v[238:239], v248 offset:7168
	v_max3_f32 v249, v249, v101, v102
	v_mfma_f32_32x32x16_bf16 v[50:65], v[26:29], v[212:215], v[50:65]
	ds_read_b64_tr_b16 v[198:199], v248 offset:9216
	ds_read_b64_tr_b16 v[200:201], v248 offset:11264
	v_max3_f32 v174, v174, v117, v118
	s_waitcnt lgkmcnt(4)
	v_mfma_f32_32x32x16_bf16 v[50:65], v[30:33], v[216:219], v[50:65]
	ds_read_b64_tr_b16 v[212:213], v248 offset:13312
	ds_read_b64_tr_b16 v[214:215], v248 offset:15360
	v_max3_f32 v249, v249, v103, v104
	v_mfma_f32_32x32x16_bf16 v[34:49], v[18:21], v[220:223], v[34:49]
	ds_read_b64_tr_b16 v[216:217], v248 offset:1536
	ds_read_b64_tr_b16 v[218:219], v248 offset:3584
	v_max3_f32 v174, v174, v119, v120
	s_waitcnt lgkmcnt(4)
	v_mfma_f32_32x32x16_bf16 v[34:49], v[22:25], v[236:239], v[34:49]
	ds_read_b64_tr_b16 v[220:221], v248 offset:5632
	ds_read_b64_tr_b16 v[222:223], v248 offset:7680
	v_max3_f32 v249, v249, v105, v106
	v_mfma_f32_32x32x16_bf16 v[34:49], v[26:29], v[198:201], v[34:49]
	ds_read_b64_tr_b16 v[236:237], v248 offset:9728
	ds_read_b64_tr_b16 v[238:239], v248 offset:11776
	v_max3_f32 v174, v174, v121, v122
	s_waitcnt lgkmcnt(4)
	v_mfma_f32_32x32x16_bf16 v[34:49], v[30:33], v[212:215], v[34:49]
	ds_read_b64_tr_b16 v[198:199], v248 offset:13824
	ds_read_b64_tr_b16 v[200:201], v248 offset:15872
	v_max3_f32 v249, v249, v107, v108
	v_mfma_f32_32x32x16_bf16 v[2:17], v[18:21], v[216:219], v[2:17]
	v_max3_f32 v174, v174, v123, v124
	s_min_u32 s14, s90, 0x7c
	s_lshl_b32 s14, s14, 17
	s_add_i32 s19, s14, 0x60000
	s_add_i32 s92, s36, 0xffff0000
	s_mov_b32 s14, s10
	s_mov_b32 s15, s11
	buffer_load_dwordx4 v[224:227], v171, s[8:11], s19 offen
	s_waitcnt lgkmcnt(2)
	v_mfma_f32_32x32x16_bf16 v[2:17], v[22:25], v[220:223], v[2:17]
	v_max3_f32 v249, v249, v109, v110
	buffer_load_dwordx4 v[228:231], v172, s[12:15], s92 offen
	v_mfma_f32_32x32x16_bf16 v[2:17], v[26:29], v[236:239], v[2:17]
	v_max3_f32 v174, v174, v125, v126
	buffer_load_dwordx4 v[232:235], v172, s[12:15], s36 offen
	s_waitcnt lgkmcnt(0)
	v_mfma_f32_32x32x16_bf16 v[2:17], v[30:33], v[198:201], v[2:17]
	v_max3_f32 v249, v249, v111, v112
	v_mfma_f32_4x4x4_16b_bf16 v[240:243], v[18:19], v[132:133], v[240:243]
	v_max3_f32 v174, v174, v127, v128
	v_mfma_f32_4x4x4_16b_bf16 v[244:247], v[20:21], v[132:133], v[244:247]
	v_mfma_f32_4x4x4_16b_bf16 v[240:243], v[22:23], v[132:133], v[240:243]
	v_max_f32 v249, v249, v113
	v_mfma_f32_4x4x4_16b_bf16 v[244:247], v[24:25], v[132:133], v[244:247]
	v_mfma_f32_4x4x4_16b_bf16 v[240:243], v[26:27], v[132:133], v[240:243]
	v_max_f32 v174, v174, v129
	v_mfma_f32_4x4x4_16b_bf16 v[244:247], v[28:29], v[132:133], v[244:247]
	v_mfma_f32_4x4x4_16b_bf16 v[240:243], v[30:31], v[132:133], v[240:243]
	v_max_f32 v174, v174, v249
	v_mfma_f32_4x4x4_16b_bf16 v[244:247], v[32:33], v[132:133], v[244:247]
	s_setprio 0
	s_barrier
	s_add_i32 s36, s36, 0x20000
	s_add_i32 s90, s90, 1
	s_cmpk_eq_i32 s90, 0x7e
	s_cbranch_scc1 .LBB0_305
	s_mov_b32 s14, s49
	s_mov_b32 s49, s51
	s_mov_b32 s51, s18
	s_mov_b32 s15, s50
	s_mov_b32 s50, s48
	s_mov_b32 s48, s37
	s_branch .LBB0_297
